# agg gather: when the batch in flight and the next are both full, rows are consumed and refilled slot by slot (8 rows stay in flight across batches)
# speedup vs baseline: 1.0050x; 1.0050x over previous
.Lagg_chk:
	s_sub_u32 s17, s14, s15
	s_cmp_ge_u32 s17, 16
	s_cbranch_scc1 .Lagg_pipe
	s_cmp_ge_u32 s16, 8
	s_cbranch_scc1 .Lagg_ac7
	s_cmp_ge_u32 s16, 7
	s_cbranch_scc1 .Lagg_ac6
	s_cmp_ge_u32 s16, 6
	s_cbranch_scc1 .Lagg_ac5
	s_cmp_ge_u32 s16, 5
	s_cbranch_scc1 .Lagg_ac4
	s_cmp_ge_u32 s16, 4
	s_cbranch_scc1 .Lagg_ac3
	s_cmp_ge_u32 s16, 3
	s_cbranch_scc1 .Lagg_ac2
	s_cmp_ge_u32 s16, 2
	s_cbranch_scc1 .Lagg_ac1
	s_branch .Lagg_ac0

.Lagg_ac0:
	s_waitcnt vmcnt(0)
	v_cvt_f32_i32_sdwa v2, sext(v40) dst_sel:DWORD dst_unused:UNUSED_PAD src0_sel:BYTE_0
	v_cvt_f32_i32_sdwa v3, sext(v40) dst_sel:DWORD dst_unused:UNUSED_PAD src0_sel:BYTE_1
	v_cvt_f32_i32_sdwa v22, sext(v40) dst_sel:DWORD dst_unused:UNUSED_PAD src0_sel:BYTE_2
	v_cvt_f32_i32_sdwa v23, sext(v40) dst_sel:DWORD dst_unused:UNUSED_PAD src0_sel:BYTE_3
	v_cvt_f32_i32_sdwa v26, sext(v41) dst_sel:DWORD dst_unused:UNUSED_PAD src0_sel:BYTE_0
	v_cvt_f32_i32_sdwa v27, sext(v41) dst_sel:DWORD dst_unused:UNUSED_PAD src0_sel:BYTE_1
	v_cvt_f32_i32_sdwa v28, sext(v41) dst_sel:DWORD dst_unused:UNUSED_PAD src0_sel:BYTE_2
	v_cvt_f32_i32_sdwa v29, sext(v41) dst_sel:DWORD dst_unused:UNUSED_PAD src0_sel:BYTE_3
	v_pk_fma_f32 v[16:17], v[32:33], v[2:3], v[16:17] op_sel_hi:[0,1,1]
	v_pk_fma_f32 v[14:15], v[32:33], v[22:23], v[14:15] op_sel_hi:[0,1,1]
	v_pk_fma_f32 v[12:13], v[32:33], v[26:27], v[12:13] op_sel_hi:[0,1,1]
	v_pk_fma_f32 v[10:11], v[32:33], v[28:29], v[10:11] op_sel_hi:[0,1,1]
	s_add_u32 s15, s15, 8
	s_cmp_lt_u32 s15, s14
	s_cbranch_scc1 .Lagg_inner
	s_add_u32 s3, s3, 64
	s_cmp_lt_u32 s3, s2
	s_cbranch_scc1 .Lagg_outer
	s_branch .LBB1_26
.Lagg_pipe:
	s_waitcnt vmcnt(14)
	v_cvt_f32_i32_sdwa v2, sext(v54) dst_sel:DWORD dst_unused:UNUSED_PAD src0_sel:BYTE_0
	v_cvt_f32_i32_sdwa v3, sext(v54) dst_sel:DWORD dst_unused:UNUSED_PAD src0_sel:BYTE_1
	v_cvt_f32_i32_sdwa v22, sext(v54) dst_sel:DWORD dst_unused:UNUSED_PAD src0_sel:BYTE_2
	v_cvt_f32_i32_sdwa v23, sext(v54) dst_sel:DWORD dst_unused:UNUSED_PAD src0_sel:BYTE_3
	v_cvt_f32_i32_sdwa v26, sext(v55) dst_sel:DWORD dst_unused:UNUSED_PAD src0_sel:BYTE_0
	v_cvt_f32_i32_sdwa v27, sext(v55) dst_sel:DWORD dst_unused:UNUSED_PAD src0_sel:BYTE_1
	v_cvt_f32_i32_sdwa v28, sext(v55) dst_sel:DWORD dst_unused:UNUSED_PAD src0_sel:BYTE_2
	v_cvt_f32_i32_sdwa v29, sext(v55) dst_sel:DWORD dst_unused:UNUSED_PAD src0_sel:BYTE_3
	v_pk_fma_f32 v[16:17], v[38:39], v[2:3], v[16:17] op_sel:[1,0,0] op_sel_hi:[1,1,1]
	v_pk_fma_f32 v[14:15], v[38:39], v[22:23], v[14:15] op_sel:[1,0,0] op_sel_hi:[1,1,1]
	v_pk_fma_f32 v[12:13], v[38:39], v[26:27], v[12:13] op_sel:[1,0,0] op_sel_hi:[1,1,1]
	v_pk_fma_f32 v[10:11], v[38:39], v[28:29], v[10:11] op_sel:[1,0,0] op_sel_hi:[1,1,1]
	s_add_u32 s17, s15, 15
	v_readlane_b32 s28, v6, s17
	s_mul_i32 s29, s28, 0x220
	s_add_u32 s54, s26, s29
	s_addc_u32 s55, s27, 0
	global_load_dwordx2 v[54:55], v8, s[54:55]
	global_load_dword v39, v20, s[54:55] offset:512
	s_waitcnt vmcnt(14)
	v_cvt_f32_i32_sdwa v2, sext(v52) dst_sel:DWORD dst_unused:UNUSED_PAD src0_sel:BYTE_0
	v_cvt_f32_i32_sdwa v3, sext(v52) dst_sel:DWORD dst_unused:UNUSED_PAD src0_sel:BYTE_1
	v_cvt_f32_i32_sdwa v22, sext(v52) dst_sel:DWORD dst_unused:UNUSED_PAD src0_sel:BYTE_2
	v_cvt_f32_i32_sdwa v23, sext(v52) dst_sel:DWORD dst_unused:UNUSED_PAD src0_sel:BYTE_3
	v_cvt_f32_i32_sdwa v26, sext(v53) dst_sel:DWORD dst_unused:UNUSED_PAD src0_sel:BYTE_0
	v_cvt_f32_i32_sdwa v27, sext(v53) dst_sel:DWORD dst_unused:UNUSED_PAD src0_sel:BYTE_1
	v_cvt_f32_i32_sdwa v28, sext(v53) dst_sel:DWORD dst_unused:UNUSED_PAD src0_sel:BYTE_2
	v_cvt_f32_i32_sdwa v29, sext(v53) dst_sel:DWORD dst_unused:UNUSED_PAD src0_sel:BYTE_3
	v_pk_fma_f32 v[16:17], v[38:39], v[2:3], v[16:17] op_sel_hi:[0,1,1]
	v_pk_fma_f32 v[14:15], v[38:39], v[22:23], v[14:15] op_sel_hi:[0,1,1]
	v_pk_fma_f32 v[12:13], v[38:39], v[26:27], v[12:13] op_sel_hi:[0,1,1]
	v_pk_fma_f32 v[10:11], v[38:39], v[28:29], v[10:11] op_sel_hi:[0,1,1]
	s_add_u32 s17, s15, 14
	v_readlane_b32 s28, v6, s17
	s_mul_i32 s29, s28, 0x220
	s_add_u32 s52, s26, s29
	s_addc_u32 s53, s27, 0
	global_load_dwordx2 v[52:53], v8, s[52:53]
	global_load_dword v38, v20, s[52:53] offset:512
	s_waitcnt vmcnt(14)
	v_cvt_f32_i32_sdwa v2, sext(v50) dst_sel:DWORD dst_unused:UNUSED_PAD src0_sel:BYTE_0
	v_cvt_f32_i32_sdwa v3, sext(v50) dst_sel:DWORD dst_unused:UNUSED_PAD src0_sel:BYTE_1
	v_cvt_f32_i32_sdwa v22, sext(v50) dst_sel:DWORD dst_unused:UNUSED_PAD src0_sel:BYTE_2
	v_cvt_f32_i32_sdwa v23, sext(v50) dst_sel:DWORD dst_unused:UNUSED_PAD src0_sel:BYTE_3
	v_cvt_f32_i32_sdwa v26, sext(v51) dst_sel:DWORD dst_unused:UNUSED_PAD src0_sel:BYTE_0
	v_cvt_f32_i32_sdwa v27, sext(v51) dst_sel:DWORD dst_unused:UNUSED_PAD src0_sel:BYTE_1
	v_cvt_f32_i32_sdwa v28, sext(v51) dst_sel:DWORD dst_unused:UNUSED_PAD src0_sel:BYTE_2
	v_cvt_f32_i32_sdwa v29, sext(v51) dst_sel:DWORD dst_unused:UNUSED_PAD src0_sel:BYTE_3
	v_pk_fma_f32 v[16:17], v[36:37], v[2:3], v[16:17] op_sel:[1,0,0] op_sel_hi:[1,1,1]
	v_pk_fma_f32 v[14:15], v[36:37], v[22:23], v[14:15] op_sel:[1,0,0] op_sel_hi:[1,1,1]
	v_pk_fma_f32 v[12:13], v[36:37], v[26:27], v[12:13] op_sel:[1,0,0] op_sel_hi:[1,1,1]
	v_pk_fma_f32 v[10:11], v[36:37], v[28:29], v[10:11] op_sel:[1,0,0] op_sel_hi:[1,1,1]
	s_add_u32 s17, s15, 13
	v_readlane_b32 s28, v6, s17
	s_mul_i32 s29, s28, 0x220
	s_add_u32 s50, s26, s29
	s_addc_u32 s51, s27, 0
	global_load_dwordx2 v[50:51], v8, s[50:51]
	global_load_dword v37, v20, s[50:51] offset:512
	s_waitcnt vmcnt(14)
	v_cvt_f32_i32_sdwa v2, sext(v48) dst_sel:DWORD dst_unused:UNUSED_PAD src0_sel:BYTE_0
	v_cvt_f32_i32_sdwa v3, sext(v48) dst_sel:DWORD dst_unused:UNUSED_PAD src0_sel:BYTE_1
	v_cvt_f32_i32_sdwa v22, sext(v48) dst_sel:DWORD dst_unused:UNUSED_PAD src0_sel:BYTE_2
	v_cvt_f32_i32_sdwa v23, sext(v48) dst_sel:DWORD dst_unused:UNUSED_PAD src0_sel:BYTE_3
	v_cvt_f32_i32_sdwa v26, sext(v49) dst_sel:DWORD dst_unused:UNUSED_PAD src0_sel:BYTE_0
	v_cvt_f32_i32_sdwa v27, sext(v49) dst_sel:DWORD dst_unused:UNUSED_PAD src0_sel:BYTE_1
	v_cvt_f32_i32_sdwa v28, sext(v49) dst_sel:DWORD dst_unused:UNUSED_PAD src0_sel:BYTE_2
	v_cvt_f32_i32_sdwa v29, sext(v49) dst_sel:DWORD dst_unused:UNUSED_PAD src0_sel:BYTE_3
	v_pk_fma_f32 v[16:17], v[36:37], v[2:3], v[16:17] op_sel_hi:[0,1,1]
	v_pk_fma_f32 v[14:15], v[36:37], v[22:23], v[14:15] op_sel_hi:[0,1,1]
	v_pk_fma_f32 v[12:13], v[36:37], v[26:27], v[12:13] op_sel_hi:[0,1,1]
	v_pk_fma_f32 v[10:11], v[36:37], v[28:29], v[10:11] op_sel_hi:[0,1,1]
	s_add_u32 s17, s15, 12
	v_readlane_b32 s28, v6, s17
	s_mul_i32 s29, s28, 0x220
	s_add_u32 s48, s26, s29
	s_addc_u32 s49, s27, 0
	global_load_dwordx2 v[48:49], v8, s[48:49]
	global_load_dword v36, v20, s[48:49] offset:512
	s_waitcnt vmcnt(14)
	v_cvt_f32_i32_sdwa v2, sext(v46) dst_sel:DWORD dst_unused:UNUSED_PAD src0_sel:BYTE_0
	v_cvt_f32_i32_sdwa v3, sext(v46) dst_sel:DWORD dst_unused:UNUSED_PAD src0_sel:BYTE_1
	v_cvt_f32_i32_sdwa v22, sext(v46) dst_sel:DWORD dst_unused:UNUSED_PAD src0_sel:BYTE_2
	v_cvt_f32_i32_sdwa v23, sext(v46) dst_sel:DWORD dst_unused:UNUSED_PAD src0_sel:BYTE_3
	v_cvt_f32_i32_sdwa v26, sext(v47) dst_sel:DWORD dst_unused:UNUSED_PAD src0_sel:BYTE_0
	v_cvt_f32_i32_sdwa v27, sext(v47) dst_sel:DWORD dst_unused:UNUSED_PAD src0_sel:BYTE_1
	v_cvt_f32_i32_sdwa v28, sext(v47) dst_sel:DWORD dst_unused:UNUSED_PAD src0_sel:BYTE_2
	v_cvt_f32_i32_sdwa v29, sext(v47) dst_sel:DWORD dst_unused:UNUSED_PAD src0_sel:BYTE_3
	v_pk_fma_f32 v[16:17], v[34:35], v[2:3], v[16:17] op_sel:[1,0,0] op_sel_hi:[1,1,1]
	v_pk_fma_f32 v[14:15], v[34:35], v[22:23], v[14:15] op_sel:[1,0,0] op_sel_hi:[1,1,1]
	v_pk_fma_f32 v[12:13], v[34:35], v[26:27], v[12:13] op_sel:[1,0,0] op_sel_hi:[1,1,1]
	v_pk_fma_f32 v[10:11], v[34:35], v[28:29], v[10:11] op_sel:[1,0,0] op_sel_hi:[1,1,1]
	s_add_u32 s17, s15, 11
	v_readlane_b32 s28, v6, s17
	s_mul_i32 s29, s28, 0x220
	s_add_u32 s46, s26, s29
	s_addc_u32 s47, s27, 0
	global_load_dwordx2 v[46:47], v8, s[46:47]
	global_load_dword v35, v20, s[46:47] offset:512
	s_waitcnt vmcnt(14)
	v_cvt_f32_i32_sdwa v2, sext(v44) dst_sel:DWORD dst_unused:UNUSED_PAD src0_sel:BYTE_0
	v_cvt_f32_i32_sdwa v3, sext(v44) dst_sel:DWORD dst_unused:UNUSED_PAD src0_sel:BYTE_1
	v_cvt_f32_i32_sdwa v22, sext(v44) dst_sel:DWORD dst_unused:UNUSED_PAD src0_sel:BYTE_2
	v_cvt_f32_i32_sdwa v23, sext(v44) dst_sel:DWORD dst_unused:UNUSED_PAD src0_sel:BYTE_3
	v_cvt_f32_i32_sdwa v26, sext(v45) dst_sel:DWORD dst_unused:UNUSED_PAD src0_sel:BYTE_0
	v_cvt_f32_i32_sdwa v27, sext(v45) dst_sel:DWORD dst_unused:UNUSED_PAD src0_sel:BYTE_1
	v_cvt_f32_i32_sdwa v28, sext(v45) dst_sel:DWORD dst_unused:UNUSED_PAD src0_sel:BYTE_2
	v_cvt_f32_i32_sdwa v29, sext(v45) dst_sel:DWORD dst_unused:UNUSED_PAD src0_sel:BYTE_3
	v_pk_fma_f32 v[16:17], v[34:35], v[2:3], v[16:17] op_sel_hi:[0,1,1]
	v_pk_fma_f32 v[14:15], v[34:35], v[22:23], v[14:15] op_sel_hi:[0,1,1]
	v_pk_fma_f32 v[12:13], v[34:35], v[26:27], v[12:13] op_sel_hi:[0,1,1]
	v_pk_fma_f32 v[10:11], v[34:35], v[28:29], v[10:11] op_sel_hi:[0,1,1]
	s_add_u32 s17, s15, 10
	v_readlane_b32 s28, v6, s17
	s_mul_i32 s29, s28, 0x220
	s_add_u32 s44, s26, s29
	s_addc_u32 s45, s27, 0
	global_load_dwordx2 v[44:45], v8, s[44:45]
	global_load_dword v34, v20, s[44:45] offset:512
	s_waitcnt vmcnt(14)
	v_cvt_f32_i32_sdwa v2, sext(v42) dst_sel:DWORD dst_unused:UNUSED_PAD src0_sel:BYTE_0
	v_cvt_f32_i32_sdwa v3, sext(v42) dst_sel:DWORD dst_unused:UNUSED_PAD src0_sel:BYTE_1
	v_cvt_f32_i32_sdwa v22, sext(v42) dst_sel:DWORD dst_unused:UNUSED_PAD src0_sel:BYTE_2
	v_cvt_f32_i32_sdwa v23, sext(v42) dst_sel:DWORD dst_unused:UNUSED_PAD src0_sel:BYTE_3
	v_cvt_f32_i32_sdwa v26, sext(v43) dst_sel:DWORD dst_unused:UNUSED_PAD src0_sel:BYTE_0
	v_cvt_f32_i32_sdwa v27, sext(v43) dst_sel:DWORD dst_unused:UNUSED_PAD src0_sel:BYTE_1
	v_cvt_f32_i32_sdwa v28, sext(v43) dst_sel:DWORD dst_unused:UNUSED_PAD src0_sel:BYTE_2
	v_cvt_f32_i32_sdwa v29, sext(v43) dst_sel:DWORD dst_unused:UNUSED_PAD src0_sel:BYTE_3
	v_pk_fma_f32 v[16:17], v[32:33], v[2:3], v[16:17] op_sel:[1,0,0] op_sel_hi:[1,1,1]
	v_pk_fma_f32 v[14:15], v[32:33], v[22:23], v[14:15] op_sel:[1,0,0] op_sel_hi:[1,1,1]
	v_pk_fma_f32 v[12:13], v[32:33], v[26:27], v[12:13] op_sel:[1,0,0] op_sel_hi:[1,1,1]
	v_pk_fma_f32 v[10:11], v[32:33], v[28:29], v[10:11] op_sel:[1,0,0] op_sel_hi:[1,1,1]
	s_add_u32 s17, s15, 9
	v_readlane_b32 s28, v6, s17
	s_mul_i32 s29, s28, 0x220
	s_add_u32 s42, s26, s29
	s_addc_u32 s43, s27, 0
	global_load_dwordx2 v[42:43], v8, s[42:43]
	global_load_dword v33, v20, s[42:43] offset:512
	s_waitcnt vmcnt(14)
	v_cvt_f32_i32_sdwa v2, sext(v40) dst_sel:DWORD dst_unused:UNUSED_PAD src0_sel:BYTE_0
	v_cvt_f32_i32_sdwa v3, sext(v40) dst_sel:DWORD dst_unused:UNUSED_PAD src0_sel:BYTE_1
	v_cvt_f32_i32_sdwa v22, sext(v40) dst_sel:DWORD dst_unused:UNUSED_PAD src0_sel:BYTE_2
	v_cvt_f32_i32_sdwa v23, sext(v40) dst_sel:DWORD dst_unused:UNUSED_PAD src0_sel:BYTE_3
	v_cvt_f32_i32_sdwa v26, sext(v41) dst_sel:DWORD dst_unused:UNUSED_PAD src0_sel:BYTE_0
	v_cvt_f32_i32_sdwa v27, sext(v41) dst_sel:DWORD dst_unused:UNUSED_PAD src0_sel:BYTE_1
	v_cvt_f32_i32_sdwa v28, sext(v41) dst_sel:DWORD dst_unused:UNUSED_PAD src0_sel:BYTE_2
	v_cvt_f32_i32_sdwa v29, sext(v41) dst_sel:DWORD dst_unused:UNUSED_PAD src0_sel:BYTE_3
	v_pk_fma_f32 v[16:17], v[32:33], v[2:3], v[16:17] op_sel_hi:[0,1,1]
	v_pk_fma_f32 v[14:15], v[32:33], v[22:23], v[14:15] op_sel_hi:[0,1,1]
	v_pk_fma_f32 v[12:13], v[32:33], v[26:27], v[12:13] op_sel_hi:[0,1,1]
	v_pk_fma_f32 v[10:11], v[32:33], v[28:29], v[10:11] op_sel_hi:[0,1,1]
	s_add_u32 s17, s15, 8
	v_readlane_b32 s28, v6, s17
	s_mul_i32 s29, s28, 0x220
	s_add_u32 s40, s26, s29
	s_addc_u32 s41, s27, 0
	global_load_dwordx2 v[40:41], v8, s[40:41]
	global_load_dword v32, v20, s[40:41] offset:512
	s_add_u32 s15, s15, 8
	s_mov_b32 s16, 8
	s_branch .Lagg_chk
